# speedup vs baseline: 1.0005x; 1.0005x over previous
.Ldiag0_done:
	s_add_i32 s60, s45, 4
	s_and_b32 s60, s60, 28
	s_lshl_b32 s60, s60, 15
	ds_read_b128 v[144:147], v169 offset:32768
	ds_read_b128 v[148:151], v169 offset:33024
	ds_read_b128 v[152:155], v169 offset:34816
	ds_read_b128 v[156:159], v169 offset:35072
	ds_read_b128 v[224:227], v169 offset:36864
	s_waitcnt lgkmcnt(4)
	v_mfma_f32_16x16x32_bf16 v[136:139], v[64:67], v[144:147], v[136:139]
	v_mfma_f32_16x16x32_bf16 v[128:131], v[68:71], v[144:147], v[128:131]
	ds_read_b128 v[228:231], v169 offset:37120
	s_waitcnt lgkmcnt(4)
	v_mfma_f32_16x16x32_bf16 v[140:143], v[64:67], v[148:151], v[140:143]
	s_or_b32 s61, s60, 0x4000
	s_mov_b32 m0, s29
	s_nop 0
	buffer_load_dwordx4 v166, s[12:15], s61 offen lds
	v_mfma_f32_16x16x32_bf16 v[132:135], v[68:71], v[148:151], v[132:135]
	ds_read_b128 v[144:147], v169 offset:38912
	s_waitcnt lgkmcnt(4)
	v_mfma_f32_16x16x32_bf16 v[136:139], v[72:75], v[152:155], v[136:139]
	v_mfma_f32_16x16x32_bf16 v[128:131], v[76:79], v[152:155], v[128:131]
	ds_read_b128 v[148:151], v169 offset:39168
	v_and_or_b32 v237, v208, s49, v234
	v_and_or_b32 v238, v216, s49, v235
	v_max_f32_e32 v161, v237, v238
	s_waitcnt lgkmcnt(4)
	v_mfma_f32_16x16x32_bf16 v[140:143], v[72:75], v[156:159], v[140:143]
	s_or_b32 s61, s60, 0x6000
	s_mov_b32 m0, s30
	s_nop 0
	buffer_load_dwordx4 v166, s[12:15], s61 offen lds
	v_mfma_f32_16x16x32_bf16 v[132:135], v[76:79], v[156:159], v[132:135]
	ds_read_b128 v[152:155], v169 offset:40960
	v_and_or_b32 v237, v209, s49, v234
	v_and_or_b32 v238, v217, s49, v235
	v_max_f32_e32 v160, v237, v238
	s_waitcnt lgkmcnt(4)
	v_mfma_f32_16x16x32_bf16 v[136:139], v[80:83], v[224:227], v[136:139]
	v_mfma_f32_16x16x32_bf16 v[128:131], v[84:87], v[224:227], v[128:131]
	ds_read_b128 v[156:159], v169 offset:41216
	v_and_or_b32 v237, v210, s49, v234
	v_and_or_b32 v238, v218, s49, v235
	v_max_f32_e32 v162, v237, v238
	s_waitcnt lgkmcnt(4)
	v_mfma_f32_16x16x32_bf16 v[140:143], v[80:83], v[228:231], v[140:143]
	s_or_b32 s61, s60, 0xc000
	s_mov_b32 m0, s31
	s_nop 0
	buffer_load_dwordx4 v166, s[12:15], s61 offen lds
	v_mfma_f32_16x16x32_bf16 v[132:135], v[84:87], v[228:231], v[132:135]
	ds_read_b128 v[224:227], v169 offset:43008
	v_and_or_b32 v237, v211, s49, v234
	v_and_or_b32 v238, v219, s49, v235
	v_max_f32_e32 v163, v237, v238
	s_waitcnt lgkmcnt(4)
	v_mfma_f32_16x16x32_bf16 v[136:139], v[88:91], v[144:147], v[136:139]
	v_mfma_f32_16x16x32_bf16 v[128:131], v[92:95], v[144:147], v[128:131]
	ds_read_b128 v[228:231], v169 offset:43264
	v_and_or_b32 v237, v212, s49, v234
	v_and_or_b32 v238, v220, s49, v235
	v_max_f32_e32 v203, v237, v238
	s_waitcnt lgkmcnt(4)
	v_mfma_f32_16x16x32_bf16 v[140:143], v[88:91], v[148:151], v[140:143]
	s_or_b32 s61, s60, 0xe000
	s_mov_b32 m0, s33
	s_nop 0
	buffer_load_dwordx4 v166, s[12:15], s61 offen lds
	v_mfma_f32_16x16x32_bf16 v[132:135], v[92:95], v[148:151], v[132:135]
	ds_read_b128 v[144:147], v169 offset:45056
	v_and_or_b32 v237, v213, s49, v234
	v_and_or_b32 v238, v221, s49, v235
	v_max_f32_e32 v204, v237, v238
	s_waitcnt lgkmcnt(4)
	v_mfma_f32_16x16x32_bf16 v[136:139], v[96:99], v[152:155], v[136:139]
	v_mfma_f32_16x16x32_bf16 v[128:131], v[100:103], v[152:155], v[128:131]
	ds_read_b128 v[148:151], v169 offset:45312
	v_and_or_b32 v237, v214, s49, v234
	v_and_or_b32 v238, v222, s49, v235
	v_max_f32_e32 v205, v237, v238
	s_waitcnt lgkmcnt(4)
	v_mfma_f32_16x16x32_bf16 v[140:143], v[96:99], v[156:159], v[140:143]
	v_mfma_f32_16x16x32_bf16 v[132:135], v[100:103], v[156:159], v[132:135]
	ds_read_b128 v[152:155], v169 offset:47104
	v_and_or_b32 v237, v215, s49, v234
	v_and_or_b32 v238, v223, s49, v235
	v_max_f32_e32 v206, v237, v238
	s_waitcnt lgkmcnt(4)
	v_mfma_f32_16x16x32_bf16 v[136:139], v[104:107], v[224:227], v[136:139]
	v_mfma_f32_16x16x32_bf16 v[128:131], v[108:111], v[224:227], v[128:131]
	ds_read_b128 v[156:159], v169 offset:47360
	s_waitcnt lgkmcnt(4)
	v_mfma_f32_16x16x32_bf16 v[140:143], v[104:107], v[228:231], v[140:143]
	v_mfma_f32_16x16x32_bf16 v[132:135], v[108:111], v[228:231], v[132:135]
	s_waitcnt lgkmcnt(3)
	v_mfma_f32_16x16x32_bf16 v[136:139], v[112:115], v[144:147], v[136:139]
	v_mfma_f32_16x16x32_bf16 v[128:131], v[116:119], v[144:147], v[128:131]
	s_waitcnt lgkmcnt(2)
	v_mfma_f32_16x16x32_bf16 v[140:143], v[112:115], v[148:151], v[140:143]
	v_mfma_f32_16x16x32_bf16 v[132:135], v[116:119], v[148:151], v[132:135]
	s_waitcnt lgkmcnt(1)
	v_mfma_f32_16x16x32_bf16 v[136:139], v[120:123], v[152:155], v[136:139]
	v_mfma_f32_16x16x32_bf16 v[128:131], v[124:127], v[152:155], v[128:131]
	s_waitcnt lgkmcnt(0)
	v_mfma_f32_16x16x32_bf16 v[140:143], v[120:123], v[156:159], v[140:143]
	v_mfma_f32_16x16x32_bf16 v[132:135], v[124:127], v[156:159], v[132:135]
	v_lshl_or_b32 v202, v167, 2, s47
	v_add_u32_e32 v202, 0x1ff00, v202
	s_add_i32 s50, s50, -4
	s_mov_b32 s51, -1.0
	s_movk_i32 s52, 0xff80
	s_brev_b32 s53, -2
	ds_read_b128 v[144:147], v168
	ds_read_b128 v[148:151], v168 offset:256
	ds_read_b128 v[152:155], v168 offset:2048
	ds_read_b128 v[156:159], v168 offset:2304
	s_waitcnt vmcnt(0)
	s_branch .LBB3_13
